# row passes P1/P10: vmcnt wait moved from the loop head to the first consumer of the next-row loads; P2 e4m3 tiles dealt 16/18 to balance the bf16 tiles; P5 tie path stops at the row end
# speedup vs baseline: 1.0020x; 1.0020x over previous
.LBB0_103:
	v_lshl_add_u64 v[18:19], v[140:141], 0, s[18:19]
	v_add_co_u32_e32 v2, vcc, 0x2000, v18
	s_nop 1
	v_addc_co_u32_e32 v3, vcc, 0, v19, vcc
	v_add_co_u32_e32 v18, vcc, 0x3000, v18
	global_load_dwordx4 v[14:17], v[2:3], off nt
	global_load_dwordx4 v[10:13], v[2:3], off offset:1024 nt
	global_load_dwordx4 v[6:9], v[2:3], off offset:2048 nt
	s_nop 0
	global_load_dwordx4 v[2:5], v[2:3], off offset:3072 nt
	v_addc_co_u32_e32 v19, vcc, 0, v19, vcc
	global_load_dwordx4 v[30:33], v[18:19], off nt
	global_load_dwordx4 v[26:29], v[18:19], off offset:1024 nt
	global_load_dwordx4 v[22:25], v[18:19], off offset:2048 nt
	s_nop 0
	global_load_dwordx4 v[18:21], v[18:19], off offset:3072 nt
	s_waitcnt vmcnt(8)
	s_branch .Lp1_head

.Lp1_head:
	v_mul_f32_e32 v154, v127, v127
	v_mul_f32_e32 v155, v123, v123
	v_fmac_f32_e32 v154, v126, v126
	v_fmac_f32_e32 v155, v122, v122
	v_fmac_f32_e32 v154, v128, v128
	v_fmac_f32_e32 v155, v124, v124
	v_fmac_f32_e32 v154, v129, v129
	v_fmac_f32_e32 v155, v125, v125
	v_add_f32_e32 v154, v154, v155
	v_mul_f32_e32 v155, v119, v119
	v_fmac_f32_e32 v155, v118, v118
	v_fmac_f32_e32 v155, v120, v120
	v_fmac_f32_e32 v155, v121, v121
	v_add_f32_e32 v154, v155, v154
	v_mul_f32_e32 v155, v115, v115
	v_fmac_f32_e32 v155, v114, v114
	v_fmac_f32_e32 v155, v116, v116
	v_fmac_f32_e32 v155, v117, v117
	v_add_f32_e32 v154, v155, v154
	v_mul_f32_e32 v155, v111, v111
	v_fmac_f32_e32 v155, v110, v110
	v_fmac_f32_e32 v155, v112, v112
	v_fmac_f32_e32 v155, v113, v113
	v_add_f32_e32 v154, v155, v154
	v_mul_f32_e32 v155, v107, v107
	v_fmac_f32_e32 v155, v106, v106
	v_fmac_f32_e32 v155, v108, v108
	v_fmac_f32_e32 v155, v109, v109
	v_add_f32_e32 v154, v155, v154
	v_mul_f32_e32 v155, v103, v103
	v_fmac_f32_e32 v155, v102, v102
	v_fmac_f32_e32 v155, v104, v104
	v_fmac_f32_e32 v155, v105, v105
	v_add_f32_e32 v154, v155, v154
	v_mul_f32_e32 v155, v83, v83
	v_fmac_f32_e32 v155, v82, v82
	v_fmac_f32_e32 v155, v84, v84
	v_fmac_f32_e32 v155, v85, v85
	v_add_f32_e32 v154, v155, v154
	v_mov_b32_e32 v157, 0
	s_add_u32 s18, s18, 0x2000
	v_add_f32_dpp v154, v154, v154 quad_perm:[1,0,3,2] row_mask:0xf bank_mask:0xf bound_ctrl:1
	s_addc_u32 s19, s19, 0
	s_cmp_eq_u32 s18, 0x20000
	v_add_f32_dpp v154, v154, v154 quad_perm:[2,3,0,1] row_mask:0xf bank_mask:0xf bound_ctrl:1
	s_nop 1
	v_add_f32_dpp v154, v154, v154 row_half_mirror row_mask:0xf bank_mask:0xf bound_ctrl:1
	s_nop 1
	v_add_f32_dpp v154, v154, v154 row_mirror row_mask:0xf bank_mask:0xf bound_ctrl:1
	v_mov_b32_e32 v155, v154
	s_nop 1
	v_permlane16_swap_b32_e32 v154, v155
	v_add_f32_e32 v154, v154, v155
	v_mov_b32_e32 v155, v154
	s_nop 1
	v_permlane32_swap_b32_e32 v154, v155
	v_add_f32_e32 v154, v154, v155
	v_fmamk_f32 v154, v154, 0x3a000000, v152
	v_mul_f32_e32 v155, 0x4b800000, v154
	v_cmp_gt_f32_e32 vcc, s21, v154
	s_nop 1
	v_cndmask_b32_e32 v154, v154, v155, vcc
	v_rsq_f32_e32 v154, v154
	s_nop 0
	v_mul_f32_e32 v155, 0x45800000, v154
	v_cndmask_b32_e32 v154, v154, v155, vcc
	v_pk_mul_f32 v[126:127], v[126:127], v[154:155] op_sel_hi:[1,0]
	v_pk_mul_f32 v[128:129], v[128:129], v[154:155] op_sel_hi:[1,0]
	s_waitcnt lgkmcnt(13)
	v_pk_fma_f32 v[126:127], v[34:35], v[126:127], v[42:43]
	v_pk_fma_f32 v[128:129], v[36:37], v[128:129], v[44:45]
	v_med3_f32 v155, v126, s22, v153
	v_med3_f32 v156, v127, s22, v153
	v_cvt_pk_fp8_f32 v157, v155, v156
	v_med3_f32 v155, v128, s22, v153
	v_med3_f32 v156, v129, s22, v153
	v_pk_mul_f32 v[122:123], v[122:123], v[154:155] op_sel_hi:[1,0]
	v_cvt_pk_fp8_f32 v157, v155, v156 op_sel:[0,0,1]
	v_cvt_pk_bf16_f32 v126, v126, v127
	v_cvt_pk_bf16_f32 v127, v128, v129
	s_waitcnt lgkmcnt(12)
	v_pk_fma_f32 v[122:123], v[122:123], v[38:39], v[46:47]
	global_store_dwordx2 v[146:147], v[126:127], off offset:-2048
	global_store_dword v[148:149], v157, off offset:-1024
	v_med3_f32 v126, v122, s22, v153
	v_med3_f32 v127, v123, s22, v153
	v_mov_b32_e32 v128, 0
	v_cvt_pk_fp8_f32 v128, v126, v127
	v_pk_mul_f32 v[124:125], v[124:125], v[154:155] op_sel_hi:[1,0]
	v_pk_mul_f32 v[118:119], v[118:119], v[154:155] op_sel_hi:[1,0]
	v_pk_fma_f32 v[124:125], v[124:125], v[40:41], v[48:49]
	v_cvt_pk_bf16_f32 v122, v122, v123
	v_med3_f32 v126, v124, s22, v153
	v_med3_f32 v127, v125, s22, v153
	v_cvt_pk_fp8_f32 v128, v126, v127 op_sel:[0,0,1]
	v_cvt_pk_bf16_f32 v123, v124, v125
	s_waitcnt lgkmcnt(9)
	v_pk_fma_f32 v[118:119], v[118:119], v[50:51], v[58:59]
	global_store_dwordx2 v[146:147], v[122:123], off offset:-1536
	global_store_dword v[148:149], v128, off offset:-768
	v_med3_f32 v122, v118, s22, v153
	v_med3_f32 v123, v119, s22, v153
	v_mov_b32_e32 v124, 0
	v_cvt_pk_fp8_f32 v124, v122, v123
	v_pk_mul_f32 v[120:121], v[120:121], v[154:155] op_sel_hi:[1,0]
	v_pk_mul_f32 v[114:115], v[114:115], v[154:155] op_sel_hi:[1,0]
	v_pk_fma_f32 v[120:121], v[120:121], v[52:53], v[60:61]
	v_cvt_pk_bf16_f32 v118, v118, v119
	v_med3_f32 v122, v120, s22, v153
	v_med3_f32 v123, v121, s22, v153
	v_cvt_pk_fp8_f32 v124, v122, v123 op_sel:[0,0,1]
	v_cvt_pk_bf16_f32 v119, v120, v121
	s_waitcnt lgkmcnt(8)
	v_pk_fma_f32 v[114:115], v[114:115], v[54:55], v[62:63]
	global_store_dwordx2 v[146:147], v[118:119], off offset:-1024
	global_store_dword v[148:149], v124, off offset:-512
	v_med3_f32 v118, v114, s22, v153
	v_med3_f32 v119, v115, s22, v153
	v_mov_b32_e32 v120, 0
	v_cvt_pk_fp8_f32 v120, v118, v119
	v_pk_mul_f32 v[116:117], v[116:117], v[154:155] op_sel_hi:[1,0]
	v_pk_mul_f32 v[110:111], v[110:111], v[154:155] op_sel_hi:[1,0]
	v_pk_fma_f32 v[116:117], v[116:117], v[56:57], v[64:65]
	v_cvt_pk_bf16_f32 v114, v114, v115
	v_med3_f32 v118, v116, s22, v153
	v_med3_f32 v119, v117, s22, v153
	v_cvt_pk_fp8_f32 v120, v118, v119 op_sel:[0,0,1]
	v_cvt_pk_bf16_f32 v115, v116, v117
	s_waitcnt lgkmcnt(5)
	v_pk_fma_f32 v[110:111], v[110:111], v[66:67], v[74:75]
	global_store_dwordx2 v[146:147], v[114:115], off offset:-512
	global_store_dword v[148:149], v120, off offset:-256
	v_med3_f32 v114, v110, s22, v153
	v_med3_f32 v115, v111, s22, v153
	v_mov_b32_e32 v116, 0
	v_cvt_pk_fp8_f32 v116, v114, v115
	v_pk_mul_f32 v[112:113], v[112:113], v[154:155] op_sel_hi:[1,0]
	v_pk_mul_f32 v[106:107], v[106:107], v[154:155] op_sel_hi:[1,0]
	v_pk_fma_f32 v[112:113], v[112:113], v[68:69], v[76:77]
	v_cvt_pk_bf16_f32 v110, v110, v111
	v_med3_f32 v114, v112, s22, v153
	v_med3_f32 v115, v113, s22, v153
	v_cvt_pk_fp8_f32 v116, v114, v115 op_sel:[0,0,1]
	v_cvt_pk_bf16_f32 v111, v112, v113
	s_waitcnt lgkmcnt(4)
	v_pk_fma_f32 v[106:107], v[106:107], v[70:71], v[78:79]
	global_store_dwordx2 v[146:147], v[110:111], off
	global_store_dword v[148:149], v116, off
	v_med3_f32 v110, v106, s22, v153
	v_med3_f32 v111, v107, s22, v153
	v_mov_b32_e32 v112, 0
	v_cvt_pk_fp8_f32 v112, v110, v111
	v_pk_mul_f32 v[108:109], v[108:109], v[154:155] op_sel_hi:[1,0]
	v_pk_mul_f32 v[102:103], v[102:103], v[154:155] op_sel_hi:[1,0]
	v_pk_fma_f32 v[108:109], v[108:109], v[72:73], v[80:81]
	v_cvt_pk_bf16_f32 v106, v106, v107
	v_med3_f32 v110, v108, s22, v153
	v_med3_f32 v111, v109, s22, v153
	v_cvt_pk_fp8_f32 v112, v110, v111 op_sel:[0,0,1]
	v_cvt_pk_bf16_f32 v107, v108, v109
	s_waitcnt lgkmcnt(1)
	v_pk_fma_f32 v[102:103], v[102:103], v[86:87], v[94:95]
	global_store_dwordx2 v[146:147], v[106:107], off offset:512
	global_store_dword v[148:149], v112, off offset:256
	v_med3_f32 v106, v102, s22, v153
	v_med3_f32 v107, v103, s22, v153
	v_mov_b32_e32 v108, 0
	v_cvt_pk_fp8_f32 v108, v106, v107
	v_pk_mul_f32 v[104:105], v[104:105], v[154:155] op_sel_hi:[1,0]
	v_pk_mul_f32 v[82:83], v[82:83], v[154:155] op_sel_hi:[1,0]
	v_pk_fma_f32 v[104:105], v[104:105], v[88:89], v[96:97]
	v_cvt_pk_bf16_f32 v102, v102, v103
	v_med3_f32 v106, v104, s22, v153
	v_med3_f32 v107, v105, s22, v153
	v_cvt_pk_fp8_f32 v108, v106, v107 op_sel:[0,0,1]
	v_cvt_pk_bf16_f32 v103, v104, v105
	s_waitcnt lgkmcnt(0)
	v_pk_fma_f32 v[82:83], v[82:83], v[90:91], v[98:99]
	global_store_dwordx2 v[146:147], v[102:103], off offset:1024
	global_store_dword v[148:149], v108, off offset:512
	v_med3_f32 v102, v82, s22, v153
	v_med3_f32 v103, v83, s22, v153
	v_mov_b32_e32 v104, 0
	v_cvt_pk_fp8_f32 v104, v102, v103
	v_pk_mul_f32 v[84:85], v[84:85], v[154:155] op_sel_hi:[1,0]
	v_cvt_pk_bf16_f32 v82, v82, v83
	v_pk_fma_f32 v[84:85], v[84:85], v[92:93], v[100:101]
	s_nop 0
	v_med3_f32 v102, v84, s22, v153
	v_med3_f32 v103, v85, s22, v153
	v_cvt_pk_fp8_f32 v104, v102, v103 op_sel:[0,0,1]
	v_cvt_pk_bf16_f32 v83, v84, v85
	global_store_dwordx2 v[146:147], v[82:83], off offset:1536
	global_store_dword v[148:149], v104, off offset:768
	v_lshl_add_u64 v[148:149], v[148:149], 0, s[12:13]
	v_lshl_add_u64 v[146:147], v[146:147], 0, s[14:15]
	s_cbranch_scc1 .LBB0_99
	s_waitcnt vmcnt(16)
	v_mov_b32_e32 v126, v14
	v_mov_b32_e32 v127, v15
	v_mov_b32_e32 v128, v16
	v_mov_b32_e32 v129, v17
	v_mov_b32_e32 v122, v10
	v_mov_b32_e32 v123, v11
	v_mov_b32_e32 v124, v12
	v_mov_b32_e32 v125, v13
	v_mov_b32_e32 v118, v6
	v_mov_b32_e32 v119, v7
	v_mov_b32_e32 v120, v8
	v_mov_b32_e32 v121, v9
	v_mov_b32_e32 v114, v2
	v_mov_b32_e32 v115, v3
	v_mov_b32_e32 v116, v4
	v_mov_b32_e32 v117, v5
	v_mov_b32_e32 v110, v30
	v_mov_b32_e32 v111, v31
	v_mov_b32_e32 v112, v32
	v_mov_b32_e32 v113, v33
	v_mov_b32_e32 v106, v26
	v_mov_b32_e32 v107, v27
	v_mov_b32_e32 v108, v28
	v_mov_b32_e32 v109, v29
	v_mov_b32_e32 v102, v22
	v_mov_b32_e32 v103, v23
	v_mov_b32_e32 v104, v24
	v_mov_b32_e32 v105, v25
	v_mov_b32_e32 v82, v18
	v_mov_b32_e32 v83, v19
	v_mov_b32_e32 v84, v20
	v_mov_b32_e32 v85, v21
	s_cmp_eq_u32 s18, 0x1e000
	s_cbranch_scc0 .Lp1_issue
	s_branch .Lp1_head
.Lp1_issue:
	v_lshl_add_u64 v[18:19], v[140:141], 0, s[18:19]
	v_add_co_u32_e32 v2, vcc, 0x2000, v18
	s_nop 1
	v_addc_co_u32_e32 v3, vcc, 0, v19, vcc
	v_add_co_u32_e32 v18, vcc, 0x3000, v18
	global_load_dwordx4 v[14:17], v[2:3], off nt
	global_load_dwordx4 v[10:13], v[2:3], off offset:1024 nt
	global_load_dwordx4 v[6:9], v[2:3], off offset:2048 nt
	s_nop 0
	global_load_dwordx4 v[2:5], v[2:3], off offset:3072 nt
	v_addc_co_u32_e32 v19, vcc, 0, v19, vcc
	global_load_dwordx4 v[30:33], v[18:19], off nt
	global_load_dwordx4 v[26:29], v[18:19], off offset:1024 nt
	global_load_dwordx4 v[22:25], v[18:19], off offset:2048 nt
	s_nop 0
	global_load_dwordx4 v[18:21], v[18:19], off offset:3072 nt
	s_branch .Lp1_head

.LBB0_240:
	s_or_b64 exec, exec, s[18:19]
	s_cmp_lg_u32 s48, 0x100
	s_cbranch_scc1 .Lp2bal_done
	s_cmp_lt_u32 s2, 0x80
	s_cbranch_scc0 .Lp2bal_hi
	v_cmp_lt_u32_e32 vcc, 0xfff, v132
	v_mov_b32_e32 v5, 0x1100
	s_nop 0
	v_cndmask_b32_e32 v132, v132, v5, vcc
	s_branch .Lp2bal_done
.Lp2bal_hi:
	v_lshrrev_b32_e32 v5, 8, v132
	v_add_u32_e32 v6, 0xfffffe80, v132
	v_cmp_eq_u32_e32 vcc, 17, v5
	s_nop 1
	v_cndmask_b32_e32 v132, v132, v6, vcc
.Lp2bal_done:
	v_lshl_add_u32 v2, v130, 4, 0
	v_add_u32_e32 v2, 0x20408, v2
	s_mov_b64 s[6:7], 0
	s_mov_b64 s[8:9], 0x1100
	s_mov_b32 s3, 0x78787879
	v_mov_b32_e32 v3, 0x33d80000
	v_mov_b32_e32 v4, 0x34e80000
	s_branch .LBB0_242

.LBB0_247:
	s_cmp_lg_u32 s48, 0x100
	s_cbranch_scc1 .Lp2cnt_done
	s_cmp_lt_u32 s2, 0x80
	s_cselect_b32 s3, 16, 18

.LBB0_608:
	s_or_b64 exec, exec, s[18:19]
	s_and_saveexec_b64 s[12:13], s[4:5]
	v_or_b32_e32 v7, vcc_hi, v7
	v_or_b32_e32 v6, vcc_lo, v6
	v_mov_b32_e32 v134, s27
	ds_write_b64 v134, v[6:7] offset:56
	s_or_b64 exec, exec, s[12:13]
	s_cmp_lt_u32 s68, 8
	s_cbranch_scc1 .Ltie_end
	v_cmp_eq_u32_e64 s[20:21], s15, v133
	s_bcnt1_i32_b64 s22, s[20:21]
	s_add_i32 s70, s69, s22
	v_cmp_lt_u32_e32 vcc, s15, v133
	v_cmp_gt_i32_e64 s[12:13], s70, v64
	v_mov_b64_e32 v[6:7], s[20:21]
	s_and_saveexec_b64 s[18:19], s[12:13]
	s_cbranch_execz .LBB0_616
	v_subrev_u32_e32 v6, s69, v64
	v_max_i32_e32 v133, 0, v6
	v_cmp_gt_u32_e64 s[12:13], s22, v133
	v_mov_b64_e32 v[6:7], s[20:21]
	s_and_saveexec_b64 s[22:23], s[12:13]
	s_cbranch_execz .LBB0_615
	s_mov_b64 s[24:25], 0

.LBB0_672:
	s_or_b64 exec, exec, s[18:19]
	s_and_saveexec_b64 s[12:13], s[4:5]
	v_or_b32_e32 v7, vcc_hi, v7
	v_or_b32_e32 v6, vcc_lo, v6
	v_mov_b32_e32 v126, s27
	ds_write_b64 v126, v[6:7] offset:120
	s_or_b64 exec, exec, s[12:13]
	s_cmp_lt_u32 s68, 16
	s_cbranch_scc1 .Ltie_end
	v_cmp_eq_u32_e64 s[20:21], s15, v125
	s_bcnt1_i32_b64 s22, s[20:21]
	s_add_i32 s70, s69, s22
	v_cmp_lt_u32_e32 vcc, s15, v125
	v_cmp_gt_i32_e64 s[12:13], s70, v64
	v_mov_b64_e32 v[6:7], s[20:21]
	s_and_saveexec_b64 s[18:19], s[12:13]
	s_cbranch_execz .LBB0_680
	v_subrev_u32_e32 v6, s69, v64
	v_max_i32_e32 v125, 0, v6
	v_cmp_gt_u32_e64 s[12:13], s22, v125
	v_mov_b64_e32 v[6:7], s[20:21]
	s_and_saveexec_b64 s[22:23], s[12:13]
	s_cbranch_execz .LBB0_679
	s_mov_b64 s[24:25], 0

.LBB0_736:
	s_or_b64 exec, exec, s[18:19]
	s_and_saveexec_b64 s[12:13], s[4:5]
	v_or_b32_e32 v7, vcc_hi, v7
	v_or_b32_e32 v6, vcc_lo, v6
	v_mov_b32_e32 v118, s27
	ds_write_b64 v118, v[6:7] offset:184
	s_or_b64 exec, exec, s[12:13]
	s_cmp_lt_u32 s68, 24
	s_cbranch_scc1 .Ltie_end
	v_cmp_eq_u32_e64 s[20:21], s15, v117
	s_bcnt1_i32_b64 s22, s[20:21]
	s_add_i32 s70, s69, s22
	v_cmp_lt_u32_e32 vcc, s15, v117
	v_cmp_gt_i32_e64 s[12:13], s70, v64
	v_mov_b64_e32 v[6:7], s[20:21]
	s_and_saveexec_b64 s[18:19], s[12:13]
	s_cbranch_execz .LBB0_744
	v_subrev_u32_e32 v6, s69, v64
	v_max_i32_e32 v117, 0, v6
	v_cmp_gt_u32_e64 s[12:13], s22, v117
	v_mov_b64_e32 v[6:7], s[20:21]
	s_and_saveexec_b64 s[22:23], s[12:13]
	s_cbranch_execz .LBB0_743
	s_mov_b64 s[24:25], 0

.LBB0_800:
	s_or_b64 exec, exec, s[18:19]
	s_and_saveexec_b64 s[12:13], s[4:5]
	v_or_b32_e32 v7, vcc_hi, v7
	v_or_b32_e32 v6, vcc_lo, v6
	v_mov_b32_e32 v109, s27
	ds_write_b64 v109, v[6:7] offset:248
	s_or_b64 exec, exec, s[12:13]
	s_cmp_lt_u32 s68, 32
	s_cbranch_scc1 .Ltie_end
	v_cmp_eq_u32_e64 s[20:21], s15, v141
	s_bcnt1_i32_b64 s22, s[20:21]
	s_add_i32 s70, s69, s22
	v_cmp_lt_u32_e32 vcc, s15, v141
	v_cmp_gt_i32_e64 s[12:13], s70, v64
	v_mov_b64_e32 v[6:7], s[20:21]
	s_and_saveexec_b64 s[18:19], s[12:13]
	s_cbranch_execz .LBB0_808
	v_subrev_u32_e32 v6, s69, v64
	v_max_i32_e32 v109, 0, v6
	v_cmp_gt_u32_e64 s[12:13], s22, v109
	v_mov_b64_e32 v[6:7], s[20:21]
	s_and_saveexec_b64 s[22:23], s[12:13]
	s_cbranch_execz .LBB0_807
	s_mov_b64 s[24:25], 0

.LBB0_864:
	s_or_b64 exec, exec, s[18:19]
	s_and_saveexec_b64 s[12:13], s[4:5]
	v_or_b32_e32 v7, vcc_hi, v7
	v_or_b32_e32 v6, vcc_lo, v6
	v_mov_b32_e32 v102, s27
	ds_write_b64 v102, v[6:7] offset:312
	s_or_b64 exec, exec, s[12:13]
	s_cmp_lt_u32 s68, 40
	s_cbranch_scc1 .Ltie_end
	v_cmp_eq_u32_e64 s[20:21], s15, v101
	s_bcnt1_i32_b64 s22, s[20:21]
	s_add_i32 s70, s69, s22
	v_cmp_lt_u32_e32 vcc, s15, v101
	v_cmp_gt_i32_e64 s[12:13], s70, v64
	v_mov_b64_e32 v[6:7], s[20:21]
	s_and_saveexec_b64 s[18:19], s[12:13]
	s_cbranch_execz .LBB0_872
	v_subrev_u32_e32 v6, s69, v64
	v_max_i32_e32 v101, 0, v6
	v_cmp_gt_u32_e64 s[12:13], s22, v101
	v_mov_b64_e32 v[6:7], s[20:21]
	s_and_saveexec_b64 s[22:23], s[12:13]
	s_cbranch_execz .LBB0_871
	s_mov_b64 s[24:25], 0

.LBB0_928:
	s_or_b64 exec, exec, s[18:19]
	s_and_saveexec_b64 s[12:13], s[4:5]
	v_or_b32_e32 v7, vcc_hi, v7
	v_or_b32_e32 v6, vcc_lo, v6
	v_mov_b32_e32 v94, s27
	ds_write_b64 v94, v[6:7] offset:376
	s_or_b64 exec, exec, s[12:13]
	s_cmp_lt_u32 s68, 48
	s_cbranch_scc1 .Ltie_end
	v_cmp_eq_u32_e64 s[20:21], s15, v93
	s_bcnt1_i32_b64 s22, s[20:21]
	s_add_i32 s70, s69, s22
	v_cmp_lt_u32_e32 vcc, s15, v93
	v_cmp_gt_i32_e64 s[12:13], s70, v64
	v_mov_b64_e32 v[6:7], s[20:21]
	s_and_saveexec_b64 s[18:19], s[12:13]
	s_cbranch_execz .LBB0_936
	v_subrev_u32_e32 v6, s69, v64
	v_max_i32_e32 v93, 0, v6
	v_cmp_gt_u32_e64 s[12:13], s22, v93
	v_mov_b64_e32 v[6:7], s[20:21]
	s_and_saveexec_b64 s[22:23], s[12:13]
	s_cbranch_execz .LBB0_935
	s_mov_b64 s[24:25], 0

.LBB0_992:
	s_or_b64 exec, exec, s[18:19]
	s_and_saveexec_b64 s[12:13], s[4:5]
	v_or_b32_e32 v7, vcc_hi, v7
	v_or_b32_e32 v6, vcc_lo, v6
	v_mov_b32_e32 v86, s27
	ds_write_b64 v86, v[6:7] offset:440
	s_or_b64 exec, exec, s[12:13]
	s_cmp_lt_u32 s68, 56
	s_cbranch_scc1 .Ltie_end
	v_cmp_eq_u32_e64 s[20:21], s15, v85
	s_bcnt1_i32_b64 s22, s[20:21]
	s_add_i32 s70, s69, s22
	v_cmp_lt_u32_e32 vcc, s15, v85
	v_cmp_gt_i32_e64 s[12:13], s70, v64
	v_mov_b64_e32 v[6:7], s[20:21]
	s_and_saveexec_b64 s[18:19], s[12:13]
	s_cbranch_execz .LBB0_1000
	v_subrev_u32_e32 v6, s69, v64
	v_max_i32_e32 v85, 0, v6
	v_cmp_gt_u32_e64 s[12:13], s22, v85
	v_mov_b64_e32 v[6:7], s[20:21]
	s_and_saveexec_b64 s[22:23], s[12:13]
	s_cbranch_execz .LBB0_999
	s_mov_b64 s[24:25], 0

.LBB0_1056:
	s_or_b64 exec, exec, s[18:19]
	s_and_saveexec_b64 s[12:13], s[4:5]
	v_or_b32_e32 v7, vcc_hi, v7
	v_or_b32_e32 v6, vcc_lo, v6
	v_mov_b32_e32 v74, s27
	ds_write_b64 v74, v[6:7] offset:504
	s_or_b64 exec, exec, s[12:13]
	s_cmp_lt_u32 s68, 64
	s_cbranch_scc1 .Ltie_end
	v_cmp_eq_u32_e64 s[20:21], s15, v110
	s_bcnt1_i32_b64 s22, s[20:21]
	s_add_i32 s70, s69, s22
	v_cmp_lt_u32_e32 vcc, s15, v110
	v_cmp_gt_i32_e64 s[12:13], s70, v64
	v_mov_b64_e32 v[6:7], s[20:21]
	s_and_saveexec_b64 s[18:19], s[12:13]
	s_cbranch_execz .LBB0_1064
	v_subrev_u32_e32 v6, s69, v64
	v_max_i32_e32 v74, 0, v6
	v_cmp_gt_u32_e64 s[12:13], s22, v74
	v_mov_b64_e32 v[6:7], s[20:21]
	s_and_saveexec_b64 s[22:23], s[12:13]
	s_cbranch_execz .LBB0_1063
	s_mov_b64 s[24:25], 0

.LBB0_1120:
	s_or_b64 exec, exec, s[18:19]
	s_and_saveexec_b64 s[12:13], s[4:5]
	v_or_b32_e32 v7, vcc_hi, v7
	v_or_b32_e32 v6, vcc_lo, v6
	v_mov_b32_e32 v70, s27
	ds_write_b64 v70, v[6:7] offset:568
	s_or_b64 exec, exec, s[12:13]
	s_cmp_lt_u32 s68, 72
	s_cbranch_scc1 .Ltie_end
	v_cmp_eq_u32_e64 s[20:21], s15, v69
	s_bcnt1_i32_b64 s22, s[20:21]
	s_add_i32 s70, s69, s22
	v_cmp_lt_u32_e32 vcc, s15, v69
	v_cmp_gt_i32_e64 s[12:13], s70, v64
	v_mov_b64_e32 v[6:7], s[20:21]
	s_and_saveexec_b64 s[18:19], s[12:13]
	s_cbranch_execz .LBB0_1128
	v_subrev_u32_e32 v6, s69, v64
	v_max_i32_e32 v69, 0, v6
	v_cmp_gt_u32_e64 s[12:13], s22, v69
	v_mov_b64_e32 v[6:7], s[20:21]
	s_and_saveexec_b64 s[22:23], s[12:13]
	s_cbranch_execz .LBB0_1127
	s_mov_b64 s[24:25], 0

.LBB0_1184:
	s_or_b64 exec, exec, s[18:19]
	s_and_saveexec_b64 s[12:13], s[4:5]
	v_or_b32_e32 v7, vcc_hi, v7
	v_or_b32_e32 v6, vcc_lo, v6
	v_mov_b32_e32 v61, s27
	ds_write_b64 v61, v[6:7] offset:632
	s_or_b64 exec, exec, s[12:13]
	s_cmp_lt_u32 s68, 80
	s_cbranch_scc1 .Ltie_end
	v_cmp_eq_u32_e64 s[20:21], s15, v60
	s_bcnt1_i32_b64 s22, s[20:21]
	s_add_i32 s70, s69, s22
	v_cmp_lt_u32_e32 vcc, s15, v60
	v_cmp_gt_i32_e64 s[12:13], s70, v64
	v_mov_b64_e32 v[6:7], s[20:21]
	s_and_saveexec_b64 s[18:19], s[12:13]
	s_cbranch_execz .LBB0_1192
	v_subrev_u32_e32 v6, s69, v64
	v_max_i32_e32 v60, 0, v6
	v_cmp_gt_u32_e64 s[12:13], s22, v60
	v_mov_b64_e32 v[6:7], s[20:21]
	s_and_saveexec_b64 s[22:23], s[12:13]
	s_cbranch_execz .LBB0_1191
	s_mov_b64 s[24:25], 0

.LBB0_1248:
	s_or_b64 exec, exec, s[18:19]
	s_and_saveexec_b64 s[12:13], s[4:5]
	v_or_b32_e32 v7, vcc_hi, v7
	v_or_b32_e32 v6, vcc_lo, v6
	v_mov_b32_e32 v53, s27
	ds_write_b64 v53, v[6:7] offset:696
	s_or_b64 exec, exec, s[12:13]
	s_cmp_lt_u32 s68, 88
	s_cbranch_scc1 .Ltie_end
	v_cmp_eq_u32_e64 s[20:21], s15, v52
	s_bcnt1_i32_b64 s22, s[20:21]
	s_add_i32 s70, s69, s22
	v_cmp_lt_u32_e32 vcc, s15, v52
	v_cmp_gt_i32_e64 s[12:13], s70, v64
	v_mov_b64_e32 v[6:7], s[20:21]
	s_and_saveexec_b64 s[18:19], s[12:13]
	s_cbranch_execz .LBB0_1256
	v_subrev_u32_e32 v6, s69, v64
	v_max_i32_e32 v52, 0, v6
	v_cmp_gt_u32_e64 s[12:13], s22, v52
	v_mov_b64_e32 v[6:7], s[20:21]
	s_and_saveexec_b64 s[22:23], s[12:13]
	s_cbranch_execz .LBB0_1255
	s_mov_b64 s[24:25], 0

.LBB0_1312:
	s_or_b64 exec, exec, s[18:19]
	s_and_saveexec_b64 s[12:13], s[4:5]
	v_or_b32_e32 v7, vcc_hi, v7
	v_or_b32_e32 v6, vcc_lo, v6
	v_mov_b32_e32 v44, s27
	ds_write_b64 v44, v[6:7] offset:760
	s_or_b64 exec, exec, s[12:13]
	s_cmp_lt_u32 s68, 96
	s_cbranch_scc1 .Ltie_end
	v_cmp_eq_u32_e64 s[20:21], s15, v78
	s_bcnt1_i32_b64 s22, s[20:21]
	s_add_i32 s70, s69, s22
	v_cmp_lt_u32_e32 vcc, s15, v78
	v_cmp_gt_i32_e64 s[12:13], s70, v64
	v_mov_b64_e32 v[6:7], s[20:21]
	s_and_saveexec_b64 s[18:19], s[12:13]
	s_cbranch_execz .LBB0_1320
	v_subrev_u32_e32 v6, s69, v64
	v_max_i32_e32 v44, 0, v6
	v_cmp_gt_u32_e64 s[12:13], s22, v44
	v_mov_b64_e32 v[6:7], s[20:21]
	s_and_saveexec_b64 s[22:23], s[12:13]
	s_cbranch_execz .LBB0_1319
	s_mov_b64 s[24:25], 0

.LBB0_1376:
	s_or_b64 exec, exec, s[18:19]
	s_and_saveexec_b64 s[12:13], s[4:5]
	v_or_b32_e32 v7, vcc_hi, v7
	v_or_b32_e32 v6, vcc_lo, v6
	v_mov_b32_e32 v38, s27
	ds_write_b64 v38, v[6:7] offset:824
	s_or_b64 exec, exec, s[12:13]
	s_cmp_lt_u32 s68, 104
	s_cbranch_scc1 .Ltie_end
	v_cmp_eq_u32_e64 s[20:21], s15, v37
	s_bcnt1_i32_b64 s22, s[20:21]
	s_add_i32 s70, s69, s22
	v_cmp_lt_u32_e32 vcc, s15, v37
	v_cmp_gt_i32_e64 s[12:13], s70, v64
	v_mov_b64_e32 v[6:7], s[20:21]
	s_and_saveexec_b64 s[18:19], s[12:13]
	s_cbranch_execz .LBB0_1384
	v_subrev_u32_e32 v6, s69, v64
	v_max_i32_e32 v37, 0, v6
	v_cmp_gt_u32_e64 s[12:13], s22, v37
	v_mov_b64_e32 v[6:7], s[20:21]
	s_and_saveexec_b64 s[22:23], s[12:13]
	s_cbranch_execz .LBB0_1383
	s_mov_b64 s[24:25], 0

.LBB0_1440:
	s_or_b64 exec, exec, s[18:19]
	s_and_saveexec_b64 s[12:13], s[4:5]
	v_or_b32_e32 v7, vcc_hi, v7
	v_or_b32_e32 v6, vcc_lo, v6
	v_mov_b32_e32 v30, s27
	ds_write_b64 v30, v[6:7] offset:888
	s_or_b64 exec, exec, s[12:13]
	s_cmp_lt_u32 s68, 112
	s_cbranch_scc1 .Ltie_end
	v_cmp_eq_u32_e64 s[20:21], s15, v29
	s_bcnt1_i32_b64 s22, s[20:21]
	s_add_i32 s70, s69, s22
	v_cmp_lt_u32_e32 vcc, s15, v29
	v_cmp_gt_i32_e64 s[12:13], s70, v64
	v_mov_b64_e32 v[6:7], s[20:21]
	s_and_saveexec_b64 s[18:19], s[12:13]
	s_cbranch_execz .LBB0_1448
	v_subrev_u32_e32 v6, s69, v64
	v_max_i32_e32 v29, 0, v6
	v_cmp_gt_u32_e64 s[12:13], s22, v29
	v_mov_b64_e32 v[6:7], s[20:21]
	s_and_saveexec_b64 s[22:23], s[12:13]
	s_cbranch_execz .LBB0_1447
	s_mov_b64 s[24:25], 0

.LBB0_1504:
	s_or_b64 exec, exec, s[18:19]
	s_and_saveexec_b64 s[12:13], s[4:5]
	v_or_b32_e32 v7, vcc_hi, v7
	v_or_b32_e32 v6, vcc_lo, v6
	v_mov_b32_e32 v22, s27
	ds_write_b64 v22, v[6:7] offset:952
	s_or_b64 exec, exec, s[12:13]
	s_cmp_lt_u32 s68, 120
	s_cbranch_scc1 .Ltie_end
	v_cmp_eq_u32_e64 s[20:21], s15, v21
	s_bcnt1_i32_b64 s22, s[20:21]
	s_add_i32 s70, s69, s22
	v_cmp_lt_u32_e32 vcc, s15, v21
	v_cmp_gt_i32_e64 s[12:13], s70, v64
	v_mov_b64_e32 v[6:7], s[20:21]
	s_and_saveexec_b64 s[18:19], s[12:13]
	s_cbranch_execz .LBB0_1512
	v_subrev_u32_e32 v6, s69, v64
	v_max_i32_e32 v21, 0, v6
	v_cmp_gt_u32_e64 s[12:13], s22, v21
	v_mov_b64_e32 v[6:7], s[20:21]
	s_and_saveexec_b64 s[22:23], s[12:13]
	s_cbranch_execz .LBB0_1511
	s_mov_b64 s[24:25], 0

.Ltie_end:
.LBB0_1571:
	s_andn2_saveexec_b64 s[16:17], s[16:17]
	s_cbranch_execz .LBB0_1644
	v_cmp_le_u32_e64 s[22:23], s15, v7
	v_cmp_le_u32_e64 s[12:13], s15, v140
	v_cmp_le_u32_e64 s[20:21], s15, v139
	v_cmp_le_u32_e32 vcc, s15, v138
	s_and_saveexec_b64 s[18:19], s[4:5]
	s_cbranch_execz .LBB0_1574
	v_mov_b32_e32 v138, s22
	v_mov_b32_e32 v139, s23
	v_mov_b32_e32 v140, s12
	v_mov_b32_e32 v141, s13
	v_mov_b32_e32 v7, s27
	ds_write_b128 v7, v[138:141]
	v_mov_b32_e32 v138, s20
	v_mov_b32_e32 v139, s21
	v_mov_b32_e32 v140, vcc_lo
	v_mov_b32_e32 v141, vcc_hi
	ds_write_b128 v7, v[138:141] offset:16

.LBB0_2152:
	v_add_co_u32_e32 v96, vcc, 0xaaa99000, v122
	s_nop 1
	v_addc_co_u32_e32 v97, vcc, 0, v123, vcc
	v_add_co_u32_e32 v46, vcc, 0x1000, v104
	global_load_dwordx4 v[18:21], v[104:105], off nt
	global_load_dwordx4 v[22:25], v[104:105], off offset:1024 nt
	global_load_dwordx4 v[26:29], v[104:105], off offset:2048 nt
	global_load_dwordx4 v[30:33], v[104:105], off offset:3072 nt
	global_load_dwordx2 v[94:95], v[96:97], off nt
	global_load_dwordx2 v[92:93], v[96:97], off offset:512 nt
	global_load_dwordx2 v[90:91], v[96:97], off offset:1024 nt
	global_load_dwordx2 v[88:89], v[96:97], off offset:1536 nt
	v_addc_co_u32_e32 v47, vcc, 0, v105, vcc
	global_load_dwordx4 v[34:37], v[46:47], off nt
	global_load_dwordx4 v[38:41], v[46:47], off offset:1024 nt
	global_load_dwordx4 v[42:45], v[46:47], off offset:2048 nt
	s_nop 0
	global_load_dwordx4 v[46:49], v[46:47], off offset:3072 nt
	s_nop 0
	global_load_dwordx2 v[102:103], v[96:97], off offset:2048 nt
	global_load_dwordx2 v[100:101], v[96:97], off offset:2560 nt
	global_load_dwordx2 v[98:99], v[96:97], off offset:3072 nt
	s_nop 0
	global_load_dwordx2 v[96:97], v[96:97], off offset:3584 nt
	s_waitcnt vmcnt(16)
	s_branch .Lp10_head

.Lp10_head:
	v_lshlrev_b32_e32 v154, 16, v120
	v_and_b32_e32 v155, 0xffff0000, v120
	v_lshlrev_b32_e32 v152, 16, v121
	v_and_b32_e32 v153, 0xffff0000, v121
	v_pk_mul_f32 v[146:147], v[154:155], v[154:155]
	v_pk_mul_f32 v[144:145], v[152:153], v[152:153]
	v_lshlrev_b32_e32 v158, 16, v118
	v_and_b32_e32 v159, 0xffff0000, v118
	v_add_f32_e32 v146, v146, v147
	v_lshlrev_b32_e32 v156, 16, v119
	v_and_b32_e32 v157, 0xffff0000, v119
	v_pk_mul_f32 v[150:151], v[158:159], v[158:159]
	v_add_f32_e32 v144, v144, v146
	v_pk_mul_f32 v[148:149], v[156:157], v[156:157]
	v_add_f32_e32 v144, v145, v144
	v_add_f32_e32 v145, v150, v151
	v_lshlrev_b32_e32 v164, 16, v116
	v_and_b32_e32 v165, 0xffff0000, v116
	v_add_f32_e32 v145, v148, v145
	v_lshlrev_b32_e32 v160, 16, v117
	v_and_b32_e32 v161, 0xffff0000, v117
	v_pk_mul_f32 v[166:167], v[164:165], v[164:165]
	v_add_f32_e32 v145, v149, v145
	v_pk_mul_f32 v[162:163], v[160:161], v[160:161]
	v_add_f32_e32 v144, v145, v144
	v_add_f32_e32 v145, v166, v167
	v_lshlrev_b32_e32 v172, 16, v114
	v_and_b32_e32 v173, 0xffff0000, v114
	v_add_f32_e32 v145, v162, v145
	v_lshlrev_b32_e32 v168, 16, v115
	v_and_b32_e32 v169, 0xffff0000, v115
	v_pk_mul_f32 v[174:175], v[172:173], v[172:173]
	v_lshlrev_b32_e32 v180, 16, v112
	v_and_b32_e32 v181, 0xffff0000, v112
	v_add_f32_e32 v145, v163, v145
	v_pk_mul_f32 v[170:171], v[168:169], v[168:169]
	v_lshlrev_b32_e32 v176, 16, v113
	v_and_b32_e32 v177, 0xffff0000, v113
	v_pk_mul_f32 v[112:113], v[180:181], v[180:181]
	v_lshlrev_b32_e32 v186, 16, v110
	v_and_b32_e32 v187, 0xffff0000, v110
	v_add_f32_e32 v144, v145, v144
	v_add_f32_e32 v145, v174, v175
	v_pk_mul_f32 v[178:179], v[176:177], v[176:177]
	v_lshlrev_b32_e32 v182, 16, v111
	v_and_b32_e32 v183, 0xffff0000, v111
	v_pk_mul_f32 v[110:111], v[186:187], v[186:187]
	v_lshlrev_b32_e32 v192, 16, v108
	v_and_b32_e32 v193, 0xffff0000, v108
	v_add_f32_e32 v145, v170, v145
	v_add_f32_e32 v112, v112, v113
	v_pk_mul_f32 v[184:185], v[182:183], v[182:183]
	v_lshlrev_b32_e32 v188, 16, v109
	v_and_b32_e32 v189, 0xffff0000, v109
	v_pk_mul_f32 v[108:109], v[192:193], v[192:193]
	v_lshlrev_b32_e32 v198, 16, v106
	v_and_b32_e32 v199, 0xffff0000, v106
	v_add_f32_e32 v145, v171, v145
	v_add_f32_e32 v112, v178, v112
	v_add_f32_e32 v110, v110, v111
	v_pk_mul_f32 v[190:191], v[188:189], v[188:189]
	v_lshlrev_b32_e32 v194, 16, v107
	v_and_b32_e32 v195, 0xffff0000, v107
	v_pk_mul_f32 v[106:107], v[198:199], v[198:199]
	v_add_f32_e32 v144, v145, v144
	v_add_f32_e32 v112, v179, v112
	v_add_f32_e32 v110, v184, v110
	v_add_f32_e32 v108, v108, v109
	v_pk_mul_f32 v[196:197], v[194:195], v[194:195]
	v_add_f32_e32 v112, v112, v144
	v_add_f32_e32 v110, v185, v110
	v_add_f32_e32 v108, v190, v108
	v_add_f32_e32 v106, v106, v107
	v_add_f32_e32 v110, v110, v112
	v_add_f32_e32 v108, v191, v108
	v_add_f32_e32 v106, v196, v106
	v_add_f32_e32 v108, v108, v110
	v_add_f32_e32 v106, v197, v106
	v_add_f32_e32 v106, v106, v108
	v_add_u32_e32 v135, 0, v72
	ds_read_b128 v[118:121], v135
	ds_read_b128 v[136:139], v135 offset:1024
	v_add_f32_dpp v106, v106, v106 quad_perm:[1,0,3,2] row_mask:0xf bank_mask:0xf bound_ctrl:1
	ds_read_b128 v[114:117], v135 offset:2048
	ds_read_b128 v[140:143], v135 offset:3072
	v_add_f32_dpp v106, v106, v106 quad_perm:[2,3,0,1] row_mask:0xf bank_mask:0xf bound_ctrl:1
	s_add_u32 s56, s14, s10
	s_addc_u32 s57, s15, s11
	v_add_f32_dpp v106, v106, v106 row_half_mirror row_mask:0xf bank_mask:0xf bound_ctrl:1
	s_add_u32 s10, s10, 0x1000
	s_addc_u32 s11, s11, 0
	v_add_f32_dpp v106, v106, v106 row_mirror row_mask:0xf bank_mask:0xf bound_ctrl:1
	v_mov_b32_e32 v107, v106
	s_nop 1
	v_permlane16_swap_b32_e32 v106, v107
	v_add_f32_e32 v106, v106, v107
	v_mov_b32_e32 v107, v106
	s_nop 1
	v_permlane32_swap_b32_e32 v106, v107
	v_add_f32_e32 v106, v106, v107
	v_fmamk_f32 v106, v106, 0x3a000000, v126
	v_mul_f32_e32 v107, 0x4b800000, v106
	v_cmp_gt_f32_e32 vcc, s62, v106
	v_lshl_add_u64 v[104:105], v[104:105], 0, s[30:31]
	s_nop 0
	v_cndmask_b32_e32 v106, v106, v107, vcc
	v_rsq_f32_e32 v162, v106
	ds_read_b128 v[106:109], v135 offset:4096
	ds_read_b128 v[110:113], v135 offset:5120
	ds_read_b128 v[144:147], v135 offset:6144
	ds_read_b128 v[148:151], v135 offset:7168
	v_mul_f32_e32 v135, 0x45800000, v162
	v_cndmask_b32_e32 v162, v162, v135, vcc
	v_pk_mul_f32 v[154:155], v[162:163], v[154:155] op_sel_hi:[0,1]
	s_waitcnt lgkmcnt(7)
	v_pk_fma_f32 v[118:119], v[118:119], v[154:155], v[62:63]
	v_pk_mul_f32 v[62:63], v[162:163], v[152:153] op_sel_hi:[0,1]
	v_pk_fma_f32 v[120:121], v[120:121], v[62:63], v[64:65]
	v_add_co_u32_e32 v122, vcc, s63, v122
	v_pk_mul_f32 v[154:155], v[118:119], v[118:119]
	v_cvt_pk_bf16_f32 v62, v118, v119
	v_cvt_pk_bf16_f32 v63, v120, v121
	v_addc_co_u32_e32 v123, vcc, 0, v123, vcc
	v_pk_mul_f32 v[152:153], v[120:121], v[120:121]
	global_store_dwordx2 v[122:123], v[62:63], off
	v_pk_mul_f32 v[62:63], v[162:163], v[158:159] op_sel_hi:[0,1]
	v_add_f32_e32 v135, v154, v155
	s_waitcnt lgkmcnt(6)
	v_pk_fma_f32 v[136:137], v[136:137], v[62:63], v[58:59]
	v_pk_mul_f32 v[58:59], v[162:163], v[156:157] op_sel_hi:[0,1]
	v_add_f32_e32 v135, v152, v135
	v_pk_mul_f32 v[158:159], v[136:137], v[136:137]
	v_pk_fma_f32 v[138:139], v[138:139], v[58:59], v[60:61]
	v_add_f32_e32 v135, v153, v135
	v_cvt_pk_bf16_f32 v58, v136, v137
	v_cvt_pk_bf16_f32 v59, v138, v139
	v_add_f32_e32 v135, v158, v135
	v_pk_mul_f32 v[156:157], v[138:139], v[138:139]
	global_store_dwordx2 v[122:123], v[58:59], off offset:512
	v_pk_mul_f32 v[58:59], v[162:163], v[164:165] op_sel_hi:[0,1]
	v_add_f32_e32 v135, v159, v135
	s_waitcnt lgkmcnt(5)
	v_pk_fma_f32 v[64:65], v[58:59], v[114:115], v[54:55]
	v_pk_mul_f32 v[54:55], v[162:163], v[160:161] op_sel_hi:[0,1]
	v_add_f32_e32 v135, v156, v135
	v_pk_mul_f32 v[114:115], v[64:65], v[64:65]
	v_pk_fma_f32 v[62:63], v[54:55], v[116:117], v[56:57]
	v_add_f32_e32 v135, v157, v135
	v_cvt_pk_bf16_f32 v54, v64, v65
	v_cvt_pk_bf16_f32 v55, v62, v63
	v_add_f32_e32 v114, v114, v135
	v_pk_mul_f32 v[116:117], v[62:63], v[62:63]
	global_store_dwordx2 v[122:123], v[54:55], off offset:1024
	v_pk_mul_f32 v[54:55], v[162:163], v[172:173] op_sel_hi:[0,1]
	v_add_f32_e32 v114, v115, v114
	s_waitcnt lgkmcnt(4)
	v_pk_fma_f32 v[60:61], v[54:55], v[140:141], v[14:15]
	v_pk_mul_f32 v[14:15], v[162:163], v[168:169] op_sel_hi:[0,1]
	v_add_f32_e32 v114, v116, v114
	v_pk_mul_f32 v[140:141], v[60:61], v[60:61]
	v_pk_fma_f32 v[58:59], v[14:15], v[142:143], v[16:17]
	v_add_f32_e32 v114, v117, v114
	v_cvt_pk_bf16_f32 v14, v60, v61
	v_cvt_pk_bf16_f32 v15, v58, v59
	v_add_f32_e32 v114, v140, v114
	v_pk_mul_f32 v[16:17], v[58:59], v[58:59]
	global_store_dwordx2 v[122:123], v[14:15], off offset:1536
	v_pk_mul_f32 v[14:15], v[162:163], v[180:181] op_sel_hi:[0,1]
	v_add_f32_e32 v114, v141, v114
	s_waitcnt lgkmcnt(3)
	v_pk_fma_f32 v[56:57], v[14:15], v[106:107], v[50:51]
	v_pk_mul_f32 v[14:15], v[162:163], v[176:177] op_sel_hi:[0,1]
	v_add_f32_e32 v16, v16, v114
	v_pk_mul_f32 v[50:51], v[56:57], v[56:57]
	v_pk_fma_f32 v[54:55], v[14:15], v[108:109], v[52:53]
	v_add_f32_e32 v16, v17, v16
	v_cvt_pk_bf16_f32 v14, v56, v57
	v_cvt_pk_bf16_f32 v15, v54, v55
	v_add_f32_e32 v16, v50, v16
	v_pk_mul_f32 v[106:107], v[54:55], v[54:55]
	global_store_dwordx2 v[122:123], v[14:15], off offset:2048
	v_pk_mul_f32 v[14:15], v[162:163], v[186:187] op_sel_hi:[0,1]
	v_add_f32_e32 v16, v51, v16
	s_waitcnt lgkmcnt(2)
	v_pk_fma_f32 v[52:53], v[14:15], v[110:111], v[10:11]
	v_pk_mul_f32 v[10:11], v[162:163], v[182:183] op_sel_hi:[0,1]
	v_add_f32_e32 v16, v106, v16
	v_pk_mul_f32 v[108:109], v[52:53], v[52:53]
	v_pk_fma_f32 v[14:15], v[10:11], v[112:113], v[12:13]
	v_add_f32_e32 v16, v107, v16
	v_cvt_pk_bf16_f32 v10, v52, v53
	v_cvt_pk_bf16_f32 v11, v14, v15
	v_add_f32_e32 v16, v108, v16
	v_pk_mul_f32 v[12:13], v[14:15], v[14:15]
	global_store_dwordx2 v[122:123], v[10:11], off offset:2560
	v_pk_mul_f32 v[10:11], v[162:163], v[192:193] op_sel_hi:[0,1]
	v_add_f32_e32 v16, v109, v16
	s_waitcnt lgkmcnt(1)
	v_pk_fma_f32 v[10:11], v[10:11], v[144:145], v[6:7]
	v_pk_mul_f32 v[6:7], v[162:163], v[188:189] op_sel_hi:[0,1]
	v_add_f32_e32 v12, v12, v16
	v_pk_mul_f32 v[110:111], v[10:11], v[10:11]
	v_pk_fma_f32 v[8:9], v[6:7], v[146:147], v[8:9]
	v_add_f32_e32 v12, v13, v12
	v_cvt_pk_bf16_f32 v6, v10, v11
	v_cvt_pk_bf16_f32 v7, v8, v9
	v_add_f32_e32 v12, v110, v12
	v_pk_mul_f32 v[112:113], v[8:9], v[8:9]
	global_store_dwordx2 v[122:123], v[6:7], off offset:3072
	v_pk_mul_f32 v[6:7], v[162:163], v[198:199] op_sel_hi:[0,1]
	v_add_f32_e32 v12, v111, v12
	s_waitcnt lgkmcnt(0)
	v_pk_fma_f32 v[6:7], v[6:7], v[148:149], v[2:3]
	v_add_f32_e32 v12, v112, v12
	v_pk_mul_f32 v[142:143], v[6:7], v[6:7]
	v_pk_mul_f32 v[2:3], v[162:163], v[194:195] op_sel_hi:[0,1]
	v_add_f32_e32 v12, v113, v12
	v_pk_fma_f32 v[2:3], v[2:3], v[150:151], v[4:5]
	v_add_f32_e32 v12, v142, v12
	v_pk_mul_f32 v[4:5], v[2:3], v[2:3]
	v_add_f32_e32 v12, v143, v12
	v_add_f32_e32 v4, v4, v12
	v_add_f32_e32 v4, v5, v4
	v_mov_b32_e32 v50, v124
	v_mov_b32_e32 v114, 0
	v_add_f32_dpp v4, v4, v4 quad_perm:[1,0,3,2] row_mask:0xf bank_mask:0xf bound_ctrl:1
	s_nop 1
	v_add_f32_dpp v4, v4, v4 quad_perm:[2,3,0,1] row_mask:0xf bank_mask:0xf bound_ctrl:1
	s_nop 1
	v_add_f32_dpp v4, v4, v4 row_half_mirror row_mask:0xf bank_mask:0xf bound_ctrl:1
	s_nop 1
	v_add_f32_dpp v4, v4, v4 row_mirror row_mask:0xf bank_mask:0xf bound_ctrl:1
	v_mov_b32_e32 v5, v4
	s_nop 1
	v_permlane16_swap_b32_e32 v4, v5
	v_add_f32_e32 v4, v4, v5
	v_mov_b32_e32 v5, v4
	s_nop 1
	v_permlane32_swap_b32_e32 v4, v5
	v_add_f32_e32 v4, v4, v5
	v_fmamk_f32 v4, v4, 0x3a000000, v126
	v_mul_f32_e32 v5, 0x4b800000, v4
	v_cmp_gt_f32_e32 vcc, s62, v4
	s_nop 1
	v_cndmask_b32_e32 v4, v4, v5, vcc
	v_rsq_f32_e32 v12, v4
	v_cvt_pk_bf16_f32 v4, v6, v7
	v_cvt_pk_bf16_f32 v5, v2, v3
	global_store_dwordx2 v[122:123], v[4:5], off offset:3584
	v_mul_f32_e32 v4, 0x45800000, v12
	v_lshl_add_u32 v5, v50, 2, 0
	v_add_u32_e32 v16, 0x4000, v5
	v_add_u32_e32 v51, 0x6000, v5
	ds_read2_b32 v[16:17], v16 offset1:1
	ds_read2_b32 v[106:107], v51 offset1:1
	v_add_u32_e32 v51, 0x4008, v5
	v_add_u32_e32 v110, 0x6008, v5
	v_cndmask_b32_e32 v4, v12, v4, vcc
	ds_read2_b32 v[108:109], v51 offset1:1
	ds_read2_b32 v[110:111], v110 offset1:1
	v_pk_mul_f32 v[12:13], v[118:119], v[4:5] op_sel_hi:[1,0]
	v_pk_mul_f32 v[112:113], v[120:121], v[4:5] op_sel_hi:[1,0]
	s_waitcnt lgkmcnt(2)
	v_pk_fma_f32 v[16:17], v[16:17], v[12:13], v[106:107]
	v_pk_mul_f32 v[116:117], v[138:139], v[4:5] op_sel_hi:[1,0]
	v_cvt_pk_bf16_f32 v51, v16, 0
	v_cvt_pk_bf16_f32 v12, v17, 0
	v_lshlrev_b32_e32 v13, 16, v12
	v_lshlrev_b32_e32 v12, 16, v51
	v_pk_add_f32 v[106:107], v[16:17], v[12:13] neg_lo:[0,1] neg_hi:[0,1]
	s_waitcnt lgkmcnt(0)
	v_pk_fma_f32 v[108:109], v[108:109], v[112:113], v[110:111]
	v_med3_f32 v16, v16, s68, v132
	v_med3_f32 v17, v17, s68, v132
	v_cvt_pk_bf16_f32 v12, v108, 0
	v_cvt_pk_bf16_f32 v110, v109, 0
	v_cvt_pk_fp8_f32 v114, v16, v17
	v_lshlrev_b32_e32 v111, 16, v110
	v_lshlrev_b32_e32 v110, 16, v12
	v_pk_add_f32 v[112:113], v[108:109], v[110:111] neg_lo:[0,1] neg_hi:[0,1]
	v_and_or_b32 v110, v51, s64, v13
	v_ashrrev_i32_e32 v51, 31, v50
	v_cvt_pk_bf16_f32 v106, v106, v107
	v_cvt_pk_bf16_f32 v107, v112, v113
	v_lshl_add_u64 v[112:113], v[50:51], 1, s[56:57]
	v_med3_f32 v16, v108, s68, v132
	v_med3_f32 v17, v109, s68, v132
	v_and_or_b32 v111, v12, s64, v111
	v_add_co_u32_e32 v12, vcc, s65, v112
	v_cvt_pk_fp8_f32 v114, v16, v17 op_sel:[0,0,1]
	s_nop 0
	v_addc_co_u32_e32 v13, vcc, 0, v113, vcc
	v_add_co_u32_e32 v16, vcc, s67, v112
	v_lshl_add_u64 v[50:51], s[12:13], 0, v[50:51]
	s_nop 0
	v_addc_co_u32_e32 v17, vcc, 0, v113, vcc
	global_store_dwordx2 v[12:13], v[110:111], off
	global_store_dwordx2 v[16:17], v[106:107], off
	global_store_dword v[50:51], v114, off offset:-1024
	v_add_u32_e32 v108, 0x4400, v5
	v_add_u32_e32 v110, 0x6400, v5
	ds_read2_b32 v[108:109], v108 offset1:1
	ds_read2_b32 v[110:111], v110 offset1:1
	v_add_u32_e32 v112, 0x4408, v5
	v_add_u32_e32 v114, 0x6408, v5
	ds_read2_b32 v[112:113], v112 offset1:1
	ds_read2_b32 v[114:115], v114 offset1:1
	v_pk_mul_f32 v[106:107], v[136:137], v[4:5] op_sel_hi:[1,0]
	v_pk_mul_f32 v[64:65], v[64:65], v[4:5] op_sel_hi:[1,0]
	s_waitcnt lgkmcnt(2)
	v_pk_fma_f32 v[106:107], v[106:107], v[108:109], v[110:111]
	v_pk_mul_f32 v[62:63], v[62:63], v[4:5] op_sel_hi:[1,0]
	v_cvt_pk_bf16_f32 v118, v106, 0
	v_cvt_pk_bf16_f32 v108, v107, 0
	v_lshlrev_b32_e32 v109, 16, v108
	v_lshlrev_b32_e32 v108, 16, v118
	s_waitcnt lgkmcnt(0)
	v_pk_fma_f32 v[112:113], v[116:117], v[112:113], v[114:115]
	v_pk_add_f32 v[110:111], v[106:107], v[108:109] neg_lo:[0,1] neg_hi:[0,1]
	v_cvt_pk_bf16_f32 v119, v112, 0
	v_cvt_pk_bf16_f32 v108, v113, 0
	v_lshlrev_b32_e32 v115, 16, v108
	v_lshlrev_b32_e32 v114, 16, v119
	v_pk_add_f32 v[116:117], v[112:113], v[114:115] neg_lo:[0,1] neg_hi:[0,1]
	v_med3_f32 v106, v106, s68, v132
	v_med3_f32 v107, v107, s68, v132
	v_mov_b32_e32 v114, 0
	v_cvt_pk_fp8_f32 v114, v106, v107
	v_cvt_pk_bf16_f32 v106, v110, v111
	v_med3_f32 v107, v112, s68, v132
	v_med3_f32 v110, v113, s68, v132
	v_cvt_pk_fp8_f32 v114, v107, v110 op_sel:[0,0,1]
	v_and_or_b32 v108, v118, s64, v109
	v_and_or_b32 v109, v119, s64, v115
	v_cvt_pk_bf16_f32 v107, v116, v117
	global_store_dwordx2 v[12:13], v[108:109], off offset:512
	global_store_dwordx2 v[16:17], v[106:107], off offset:512
	global_store_dword v[50:51], v114, off offset:-768
	v_add_u32_e32 v106, 0x4800, v5
	v_add_u32_e32 v108, 0x6800, v5
	ds_read2_b32 v[106:107], v106 offset1:1
	ds_read2_b32 v[108:109], v108 offset1:1
	v_add_u32_e32 v110, 0x4808, v5
	v_add_u32_e32 v112, 0x6808, v5
	ds_read2_b32 v[110:111], v110 offset1:1
	ds_read2_b32 v[112:113], v112 offset1:1
	v_pk_mul_f32 v[60:61], v[60:61], v[4:5] op_sel_hi:[1,0]
	s_waitcnt lgkmcnt(2)
	v_pk_fma_f32 v[64:65], v[64:65], v[106:107], v[108:109]
	v_pk_mul_f32 v[58:59], v[58:59], v[4:5] op_sel_hi:[1,0]
	v_cvt_pk_bf16_f32 v114, v64, 0
	v_cvt_pk_bf16_f32 v106, v65, 0
	v_lshlrev_b32_e32 v107, 16, v106
	v_lshlrev_b32_e32 v106, 16, v114
	s_waitcnt lgkmcnt(0)
	v_pk_fma_f32 v[62:63], v[62:63], v[110:111], v[112:113]
	v_pk_add_f32 v[108:109], v[64:65], v[106:107] neg_lo:[0,1] neg_hi:[0,1]
	v_cvt_pk_bf16_f32 v115, v62, 0
	v_cvt_pk_bf16_f32 v106, v63, 0
	v_lshlrev_b32_e32 v111, 16, v106
	v_lshlrev_b32_e32 v110, 16, v115
	v_pk_add_f32 v[112:113], v[62:63], v[110:111] neg_lo:[0,1] neg_hi:[0,1]
	v_med3_f32 v64, v64, s68, v132
	v_med3_f32 v65, v65, s68, v132
	v_mov_b32_e32 v110, 0
	v_cvt_pk_fp8_f32 v110, v64, v65
	v_med3_f32 v62, v62, s68, v132
	v_med3_f32 v63, v63, s68, v132
	v_and_or_b32 v106, v114, s64, v107
	v_cvt_pk_fp8_f32 v110, v62, v63 op_sel:[0,0,1]
	v_and_or_b32 v107, v115, s64, v111
	v_cvt_pk_bf16_f32 v64, v108, v109
	v_cvt_pk_bf16_f32 v65, v112, v113
	global_store_dwordx2 v[12:13], v[106:107], off offset:1024
	global_store_dwordx2 v[16:17], v[64:65], off offset:1024
	global_store_dword v[50:51], v110, off offset:-512
	v_add_u32_e32 v62, 0x4c00, v5
	v_add_u32_e32 v64, 0x6c00, v5
	ds_read2_b32 v[62:63], v62 offset1:1
	ds_read2_b32 v[64:65], v64 offset1:1
	v_add_u32_e32 v106, 0x4c08, v5
	v_add_u32_e32 v108, 0x6c08, v5
	ds_read2_b32 v[106:107], v106 offset1:1
	ds_read2_b32 v[108:109], v108 offset1:1
	v_pk_mul_f32 v[56:57], v[56:57], v[4:5] op_sel_hi:[1,0]
	s_waitcnt lgkmcnt(2)
	v_pk_fma_f32 v[60:61], v[60:61], v[62:63], v[64:65]
	v_pk_mul_f32 v[54:55], v[54:55], v[4:5] op_sel_hi:[1,0]
	v_cvt_pk_bf16_f32 v110, v60, 0
	v_cvt_pk_bf16_f32 v62, v61, 0
	v_lshlrev_b32_e32 v63, 16, v62
	v_lshlrev_b32_e32 v62, 16, v110
	s_waitcnt lgkmcnt(0)
	v_pk_fma_f32 v[58:59], v[58:59], v[106:107], v[108:109]
	v_pk_add_f32 v[64:65], v[60:61], v[62:63] neg_lo:[0,1] neg_hi:[0,1]
	v_cvt_pk_bf16_f32 v111, v58, 0
	v_cvt_pk_bf16_f32 v62, v59, 0
	v_lshlrev_b32_e32 v107, 16, v62
	v_lshlrev_b32_e32 v106, 16, v111
	v_pk_add_f32 v[108:109], v[58:59], v[106:107] neg_lo:[0,1] neg_hi:[0,1]
	v_med3_f32 v60, v60, s68, v132
	v_med3_f32 v61, v61, s68, v132
	v_mov_b32_e32 v106, 0
	v_cvt_pk_fp8_f32 v106, v60, v61
	v_med3_f32 v58, v58, s68, v132
	v_med3_f32 v59, v59, s68, v132
	v_and_or_b32 v62, v110, s64, v63
	v_cvt_pk_fp8_f32 v106, v58, v59 op_sel:[0,0,1]
	v_and_or_b32 v63, v111, s64, v107
	v_cvt_pk_bf16_f32 v60, v64, v65
	v_cvt_pk_bf16_f32 v61, v108, v109
	global_store_dwordx2 v[12:13], v[62:63], off offset:1536
	global_store_dwordx2 v[16:17], v[60:61], off offset:1536
	global_store_dword v[50:51], v106, off offset:-256
	v_add_u32_e32 v58, 0x5000, v5
	v_add_u32_e32 v60, 0x7000, v5
	ds_read2_b32 v[58:59], v58 offset1:1
	ds_read2_b32 v[60:61], v60 offset1:1
	v_add_u32_e32 v62, 0x5008, v5
	v_add_u32_e32 v64, 0x7008, v5
	ds_read2_b32 v[62:63], v62 offset1:1
	ds_read2_b32 v[64:65], v64 offset1:1
	v_pk_mul_f32 v[52:53], v[52:53], v[4:5] op_sel_hi:[1,0]
	s_waitcnt lgkmcnt(2)
	v_pk_fma_f32 v[56:57], v[56:57], v[58:59], v[60:61]
	v_pk_mul_f32 v[14:15], v[14:15], v[4:5] op_sel_hi:[1,0]
	v_cvt_pk_bf16_f32 v106, v56, 0
	v_cvt_pk_bf16_f32 v58, v57, 0
	v_lshlrev_b32_e32 v59, 16, v58
	v_lshlrev_b32_e32 v58, 16, v106
	s_waitcnt lgkmcnt(0)
	v_pk_fma_f32 v[54:55], v[54:55], v[62:63], v[64:65]
	v_pk_add_f32 v[60:61], v[56:57], v[58:59] neg_lo:[0,1] neg_hi:[0,1]
	v_cvt_pk_bf16_f32 v107, v54, 0
	v_cvt_pk_bf16_f32 v58, v55, 0
	v_lshlrev_b32_e32 v63, 16, v58
	v_lshlrev_b32_e32 v62, 16, v107
	v_pk_add_f32 v[64:65], v[54:55], v[62:63] neg_lo:[0,1] neg_hi:[0,1]
	v_med3_f32 v56, v56, s68, v132
	v_med3_f32 v57, v57, s68, v132
	v_mov_b32_e32 v62, 0
	v_cvt_pk_fp8_f32 v62, v56, v57
	v_med3_f32 v54, v54, s68, v132
	v_med3_f32 v55, v55, s68, v132
	v_and_or_b32 v58, v106, s64, v59
	v_cvt_pk_fp8_f32 v62, v54, v55 op_sel:[0,0,1]
	v_and_or_b32 v59, v107, s64, v63
	v_cvt_pk_bf16_f32 v56, v60, v61
	v_cvt_pk_bf16_f32 v57, v64, v65
	global_store_dwordx2 v[12:13], v[58:59], off offset:2048
	global_store_dwordx2 v[16:17], v[56:57], off offset:2048
	global_store_dword v[50:51], v62, off
	v_add_u32_e32 v54, 0x5400, v5
	v_add_u32_e32 v56, 0x7400, v5
	ds_read2_b32 v[54:55], v54 offset1:1
	ds_read2_b32 v[56:57], v56 offset1:1
	v_add_u32_e32 v58, 0x5408, v5
	v_add_u32_e32 v60, 0x7408, v5
	ds_read2_b32 v[58:59], v58 offset1:1
	ds_read2_b32 v[60:61], v60 offset1:1
	v_pk_mul_f32 v[10:11], v[10:11], v[4:5] op_sel_hi:[1,0]
	s_waitcnt lgkmcnt(2)
	v_pk_fma_f32 v[52:53], v[52:53], v[54:55], v[56:57]
	v_pk_mul_f32 v[8:9], v[8:9], v[4:5] op_sel_hi:[1,0]
	v_cvt_pk_bf16_f32 v62, v52, 0
	v_cvt_pk_bf16_f32 v54, v53, 0
	v_lshlrev_b32_e32 v55, 16, v54
	v_lshlrev_b32_e32 v54, 16, v62
	s_waitcnt lgkmcnt(0)
	v_pk_fma_f32 v[14:15], v[14:15], v[58:59], v[60:61]
	v_pk_add_f32 v[56:57], v[52:53], v[54:55] neg_lo:[0,1] neg_hi:[0,1]
	v_cvt_pk_bf16_f32 v63, v14, 0
	v_cvt_pk_bf16_f32 v54, v15, 0
	v_lshlrev_b32_e32 v59, 16, v54
	v_lshlrev_b32_e32 v58, 16, v63
	v_pk_add_f32 v[60:61], v[14:15], v[58:59] neg_lo:[0,1] neg_hi:[0,1]
	v_med3_f32 v52, v52, s68, v132
	v_med3_f32 v53, v53, s68, v132
	v_mov_b32_e32 v58, 0
	v_cvt_pk_fp8_f32 v58, v52, v53
	v_med3_f32 v14, v14, s68, v132
	v_med3_f32 v15, v15, s68, v132
	v_and_or_b32 v54, v62, s64, v55
	v_cvt_pk_fp8_f32 v58, v14, v15 op_sel:[0,0,1]
	v_and_or_b32 v55, v63, s64, v59
	v_cvt_pk_bf16_f32 v52, v56, v57
	v_cvt_pk_bf16_f32 v53, v60, v61
	global_store_dwordx2 v[12:13], v[54:55], off offset:2560
	global_store_dwordx2 v[16:17], v[52:53], off offset:2560
	global_store_dword v[50:51], v58, off offset:256
	v_add_u32_e32 v14, 0x5800, v5
	v_add_u32_e32 v52, 0x7800, v5
	ds_read2_b32 v[14:15], v14 offset1:1
	ds_read2_b32 v[52:53], v52 offset1:1
	v_add_u32_e32 v54, 0x5808, v5
	v_add_u32_e32 v56, 0x7808, v5
	ds_read2_b32 v[54:55], v54 offset1:1
	ds_read2_b32 v[56:57], v56 offset1:1
	v_pk_mul_f32 v[6:7], v[6:7], v[4:5] op_sel_hi:[1,0]
	s_waitcnt lgkmcnt(2)
	v_pk_fma_f32 v[10:11], v[10:11], v[14:15], v[52:53]
	s_add_u32 s12, s12, 0x800
	v_cvt_pk_bf16_f32 v58, v10, 0
	v_cvt_pk_bf16_f32 v14, v11, 0
	v_lshlrev_b32_e32 v15, 16, v14
	v_lshlrev_b32_e32 v14, 16, v58
	s_waitcnt lgkmcnt(0)
	v_pk_fma_f32 v[8:9], v[8:9], v[54:55], v[56:57]
	v_pk_add_f32 v[52:53], v[10:11], v[14:15] neg_lo:[0,1] neg_hi:[0,1]
	v_cvt_pk_bf16_f32 v59, v8, 0
	v_cvt_pk_bf16_f32 v14, v9, 0
	v_lshlrev_b32_e32 v55, 16, v14
	v_lshlrev_b32_e32 v54, 16, v59
	v_pk_add_f32 v[56:57], v[8:9], v[54:55] neg_lo:[0,1] neg_hi:[0,1]
	v_med3_f32 v10, v10, s68, v132
	v_med3_f32 v11, v11, s68, v132
	v_mov_b32_e32 v54, 0
	v_cvt_pk_fp8_f32 v54, v10, v11
	v_med3_f32 v8, v8, s68, v132
	v_med3_f32 v9, v9, s68, v132
	v_and_or_b32 v14, v58, s64, v15
	v_cvt_pk_fp8_f32 v54, v8, v9 op_sel:[0,0,1]
	v_and_or_b32 v15, v59, s64, v55
	v_cvt_pk_bf16_f32 v10, v52, v53
	v_cvt_pk_bf16_f32 v11, v56, v57
	global_store_dwordx2 v[12:13], v[14:15], off offset:3072
	global_store_dwordx2 v[16:17], v[10:11], off offset:3072
	global_store_dword v[50:51], v54, off offset:512
	v_add_u32_e32 v8, 0x5c00, v5
	v_add_u32_e32 v10, 0x7c00, v5
	ds_read2_b32 v[8:9], v8 offset1:1
	ds_read2_b32 v[10:11], v10 offset1:1
	v_add_u32_e32 v14, 0x5c08, v5
	v_add_u32_e32 v5, 0x7c08, v5
	ds_read2_b32 v[14:15], v14 offset1:1
	ds_read2_b32 v[52:53], v5 offset1:1
	s_addc_u32 s13, s13, 0
	s_waitcnt lgkmcnt(2)
	v_pk_fma_f32 v[6:7], v[6:7], v[8:9], v[10:11]
	s_cmp_eq_u32 s10, 0x10000
	v_cvt_pk_bf16_f32 v5, v7, 0
	v_cvt_pk_bf16_f32 v54, v6, 0
	v_pk_mul_f32 v[2:3], v[2:3], v[4:5] op_sel_hi:[1,0]
	v_lshlrev_b32_e32 v9, 16, v5
	v_lshlrev_b32_e32 v8, 16, v54
	s_waitcnt lgkmcnt(0)
	v_pk_fma_f32 v[2:3], v[2:3], v[14:15], v[52:53]
	v_pk_add_f32 v[10:11], v[6:7], v[8:9] neg_lo:[0,1] neg_hi:[0,1]
	v_cvt_pk_bf16_f32 v8, v2, 0
	v_cvt_pk_bf16_f32 v4, v3, 0
	v_lshlrev_b32_e32 v5, 16, v4
	v_lshlrev_b32_e32 v4, 16, v8
	v_pk_add_f32 v[14:15], v[2:3], v[4:5] neg_lo:[0,1] neg_hi:[0,1]
	v_and_or_b32 v5, v8, s64, v5
	v_med3_f32 v6, v6, s68, v132
	v_med3_f32 v7, v7, s68, v132
	v_mov_b32_e32 v8, 0
	v_cvt_pk_fp8_f32 v8, v6, v7
	v_med3_f32 v2, v2, s68, v132
	v_med3_f32 v3, v3, s68, v132
	v_and_or_b32 v4, v54, s64, v9
	v_cvt_pk_fp8_f32 v8, v2, v3 op_sel:[0,0,1]
	v_cvt_pk_bf16_f32 v6, v10, v11
	v_cvt_pk_bf16_f32 v7, v14, v15
	global_store_dwordx2 v[12:13], v[4:5], off offset:3584
	global_store_dwordx2 v[16:17], v[6:7], off offset:3584
	global_store_dword v[50:51], v8, off offset:768
	s_cbranch_scc1 .LBB0_2155
	s_waitcnt vmcnt(32)
	v_mov_b64_e32 v[106:107], v[96:97]
	v_mov_b64_e32 v[108:109], v[98:99]
	v_mov_b64_e32 v[110:111], v[100:101]
	v_mov_b64_e32 v[112:113], v[102:103]
	v_mov_b64_e32 v[114:115], v[88:89]
	v_mov_b64_e32 v[116:117], v[90:91]
	v_mov_b64_e32 v[118:119], v[92:93]
	v_mov_b64_e32 v[120:121], v[94:95]
	v_mov_b32_e32 v62, v18
	v_mov_b32_e32 v63, v19
	v_mov_b32_e32 v64, v20
	v_mov_b32_e32 v65, v21
	v_mov_b32_e32 v58, v22
	v_mov_b32_e32 v59, v23
	v_mov_b32_e32 v60, v24
	v_mov_b32_e32 v61, v25
	v_mov_b32_e32 v54, v26
	v_mov_b32_e32 v55, v27
	v_mov_b32_e32 v56, v28
	v_mov_b32_e32 v57, v29
	v_mov_b32_e32 v14, v30
	v_mov_b32_e32 v15, v31
	v_mov_b32_e32 v16, v32
	v_mov_b32_e32 v17, v33
	v_mov_b32_e32 v50, v34
	v_mov_b32_e32 v51, v35
	v_mov_b32_e32 v52, v36
	v_mov_b32_e32 v53, v37
	v_mov_b32_e32 v10, v38
	v_mov_b32_e32 v11, v39
	v_mov_b32_e32 v12, v40
	v_mov_b32_e32 v13, v41
	v_mov_b32_e32 v6, v42
	v_mov_b32_e32 v7, v43
	v_mov_b32_e32 v8, v44
	v_mov_b32_e32 v9, v45
	v_mov_b32_e32 v2, v46
	v_mov_b32_e32 v3, v47
	v_mov_b32_e32 v4, v48
	v_mov_b32_e32 v5, v49
	s_cmpk_eq_u32 s10, 0xf000
	v_lshl_add_u64 v[122:123], v[82:83], 0, s[10:11]
	s_cbranch_scc0 .Lp10_issue
	s_branch .Lp10_head
.Lp10_issue:
	v_add_co_u32_e32 v96, vcc, 0xaaa99000, v122
	s_nop 1
	v_addc_co_u32_e32 v97, vcc, 0, v123, vcc
	v_add_co_u32_e32 v46, vcc, 0x1000, v104
	global_load_dwordx4 v[18:21], v[104:105], off nt
	global_load_dwordx4 v[22:25], v[104:105], off offset:1024 nt
	global_load_dwordx4 v[26:29], v[104:105], off offset:2048 nt
	global_load_dwordx4 v[30:33], v[104:105], off offset:3072 nt
	global_load_dwordx2 v[94:95], v[96:97], off nt
	global_load_dwordx2 v[92:93], v[96:97], off offset:512 nt
	global_load_dwordx2 v[90:91], v[96:97], off offset:1024 nt
	global_load_dwordx2 v[88:89], v[96:97], off offset:1536 nt
	v_addc_co_u32_e32 v47, vcc, 0, v105, vcc
	global_load_dwordx4 v[34:37], v[46:47], off nt
	global_load_dwordx4 v[38:41], v[46:47], off offset:1024 nt
	global_load_dwordx4 v[42:45], v[46:47], off offset:2048 nt
	s_nop 0
	global_load_dwordx4 v[46:49], v[46:47], off offset:3072 nt
	s_nop 0
	global_load_dwordx2 v[102:103], v[96:97], off offset:2048 nt
	global_load_dwordx2 v[100:101], v[96:97], off offset:2560 nt
	global_load_dwordx2 v[98:99], v[96:97], off offset:3072 nt
	s_nop 0
	global_load_dwordx2 v[96:97], v[96:97], off offset:3584 nt
	s_branch .Lp10_head
